# static s_setprio 1 for waves 0-3 across the attention mainloop (other half of the strategy-4 A/B)
# baseline (speedup 1.0000x reference)
; template <int CTRL> __device__ __forceinline__ float dpp_f(float v) { return __uint_as_float((unsigned)__builtin_amdgcn_update_dpp(0, (int)__float_as_uint(v), CTRL, 0xF, 0xF, true)); }
; __device__ __forceinline__ float swap16_max(float a) { const auto r = __builtin_amdgcn_permlane16_swap(__float_as_uint(a), __float_as_uint(a), false, false); return fmaxf(__uint_as_float(r[0]), __uint_as_float(r[1])); }
; __device__ __forceinline__ float swap32_max(float a) { const auto r = __builtin_amdgcn_permlane32_swap(__float_as_uint(a), __float_as_uint(a), false, false); return fmaxf(__uint_as_float(r[0]), __uint_as_float(r[1])); }
; __global__ void __launch_bounds__(NTHR, 2) fwd_kernel(Args args) {
;     ...
;             __syncthreads();
;             float gq_ = fabsf(INP(F, I_QNORM)[l * 64 + F.lane]), gk_ = fabsf(INP(F, I_KNORM)[l * 64 + F.lane]);
;             gq_ = fmaxf(gq_, dpp_f<DPP_X1>(gq_)); gq_ = fmaxf(gq_, dpp_f<DPP_X2>(gq_)); gq_ = fmaxf(gq_, dpp_f<DPP_HMIR>(gq_)); gq_ = fmaxf(gq_, dpp_f<DPP_MIR>(gq_)); gq_ = swap16_max(gq_); gq_ = swap32_max(gq_);
;             gk_ = fmaxf(gk_, dpp_f<DPP_X1>(gk_)); gk_ = fmaxf(gk_, dpp_f<DPP_X2>(gk_)); gk_ = fmaxf(gk_, dpp_f<DPP_HMIR>(gk_)); gk_ = fmaxf(gk_, dpp_f<DPP_MIR>(gk_)); gk_ = swap16_max(gk_); gk_ = swap32_max(gk_);
;             const float mfix = __uint_as_float(__builtin_amdgcn_readfirstlane(__float_as_uint(1.02f * ATT_C2 * 64.0f * gq_ * gk_)));
;             const bool nomax = mfix <= 60.0f;
;             REPS(13) for (int i = 0; ; ++i) { const int U = split ? F.vcu + F.G * i : 2 * F.vcu + i; if (U >= 512 || (!split && i >= 2)) break;
;                     const int grp = U >> 6, j = U & 63, b = grp >> 1, h = (grp & 1) * 4 + (j >> 4), qb = j & 15;
;                     if (nomax) attn_body::attn_unit<8, true>(b, h, qb, (const attn_body::bf16*)(F.ws + WS_QP), (const attn_body::bf16*)(F.ws + WS_KV), (const attn_body::bf16*)(F.ws + WS_KV) + 128,
;                                             (attn_body::bf16*)(F.ws + WS_CAT) + 256, (char*)lds, mfix);
;                     else attn_body::attn_unit<8>(b, h, qb, (const attn_body::bf16*)(F.ws + WS_QP), (const attn_body::bf16*)(F.ws + WS_KV), (const attn_body::bf16*)(F.ws + WS_KV) + 128,
;                                             (attn_body::bf16*)(F.ws + WS_CAT) + 256, (char*)lds); }
.LBB0_711:
	v_readlane_b32 s2, v254, 36
	s_barrier
	s_nop 0
	v_mov_b32_e32 v1, s2
	s_barrier
	ds_read_b128 v[2:5], v1
	v_readlane_b32 s4, v255, 5
	s_andn2_b64 vcc, exec, s[10:11]
	s_mov_b64 s[46:47], 0x20000
	v_lshl_or_b32 v182, s4, 6, v186
	s_waitcnt lgkmcnt(0)
	v_readfirstlane_b32 s2, v2
	v_readfirstlane_b32 s3, v3
	v_lshlrev_b64 v[2:3], 2, v[182:183]
	s_waitcnt vmcnt(0)
	v_lshl_add_u64 v[6:7], s[2:3], 0, v[2:3]
	v_readfirstlane_b32 s2, v4
	v_readfirstlane_b32 s3, v5
	global_load_dword v1, v[6:7], off
	s_nop 0
	v_lshl_add_u64 v[2:3], s[2:3], 0, v[2:3]
	global_load_dword v2, v[2:3], off
	s_waitcnt vmcnt(0)
	v_and_b32_e32 v3, 0x7fffffff, v1
	s_nop 1
	v_mov_b32_dpp v3, v3 quad_perm:[1,0,3,2] row_mask:0xf bank_mask:0xf bound_ctrl:1
	v_max_f32_e64 v1, |v1|, |v1|
	v_and_b32_e32 v4, 0x7fffffff, v2
	v_max_f32_e32 v3, v3, v3
	v_max_f32_e64 v2, |v2|, |v2|
	v_mov_b32_dpp v4, v4 quad_perm:[1,0,3,2] row_mask:0xf bank_mask:0xf bound_ctrl:1
	v_max_f32_e32 v4, v4, v4
	v_max_f32_e32 v1, v1, v3
	v_max_f32_e32 v2, v2, v4
	s_nop 0
	v_mov_b32_dpp v3, v1 quad_perm:[2,3,0,1] row_mask:0xf bank_mask:0xf bound_ctrl:1
	v_mov_b32_dpp v4, v2 quad_perm:[2,3,0,1] row_mask:0xf bank_mask:0xf bound_ctrl:1
	v_max_f32_e32 v3, v3, v3
	v_max_f32_e32 v4, v4, v4
	v_max_f32_e32 v1, v1, v3
	v_max_f32_e32 v2, v2, v4
	s_nop 0
	v_mov_b32_dpp v3, v1 row_half_mirror row_mask:0xf bank_mask:0xf bound_ctrl:1
	v_mov_b32_dpp v4, v2 row_half_mirror row_mask:0xf bank_mask:0xf bound_ctrl:1
	v_max_f32_e32 v3, v3, v3
	v_max_f32_e32 v4, v4, v4
	v_max_f32_e32 v1, v1, v3
	v_max_f32_e32 v2, v2, v4
	s_nop 0
	v_mov_b32_dpp v3, v1 row_mirror row_mask:0xf bank_mask:0xf bound_ctrl:1
	v_mov_b32_dpp v4, v2 row_mirror row_mask:0xf bank_mask:0xf bound_ctrl:1
	v_max_f32_e32 v3, v3, v3
	v_max_f32_e32 v4, v4, v4
	v_max_f32_e32 v1, v1, v3
	v_max_f32_e32 v2, v2, v4
	v_mov_b32_e32 v3, v1
	v_mov_b32_e32 v4, v2
	s_nop 0
	v_permlane16_swap_b32_e32 v1, v3
	v_permlane16_swap_b32_e32 v2, v4
	v_max_f32_e32 v3, v3, v3
	v_max_f32_e32 v1, v1, v1
	v_max_f32_e32 v4, v4, v4
	v_max_f32_e32 v2, v2, v2
	v_max_f32_e32 v1, v1, v3
	v_max_f32_e32 v2, v2, v4
	v_mov_b32_e32 v3, v1
	v_mov_b32_e32 v4, v2
	s_nop 0
	v_permlane32_swap_b32_e32 v1, v3
	v_permlane32_swap_b32_e32 v2, v4
	v_max_f32_e32 v3, v3, v3
	v_max_f32_e32 v1, v1, v1
	v_max_f32_e32 v4, v4, v4
	v_max_f32_e32 v2, v2, v2
	v_max_f32_e32 v1, v1, v3
	v_max_f32_e32 v2, v2, v4
	v_mul_f32_e32 v1, 0x413c5bb7, v1
	v_mul_f32_e32 v1, v1, v2
	s_nop 0
	v_readfirstlane_b32 s34, v1
	s_cbranch_vccnz .LBB0_773
	s_lshl_b32 s3, s22, 1
	s_ashr_i32 s2, s22, 6
	s_or_b32 s35, s3, 1
	s_and_b32 s36, s3, 14
	s_ashr_i32 s3, s2, 31
	s_lshl_b64 s[8:9], s[2:3], 12
	s_lshl_b64 s[2:3], s[2:3], 21
	s_add_u32 s6, s58, s2
	s_addc_u32 s7, s59, s3
	s_lshl_b32 s10, s22, 2
	s_and_b32 s14, s10, 0x80
	s_add_u32 s6, s6, s14
	s_addc_u32 s7, s7, 0
	s_add_u32 s10, s6, 0xa400000
	s_addc_u32 s11, s7, 0
	s_add_u32 s12, s6, 0xa400100
	s_addc_u32 s13, s7, 0
	s_lshl_b32 s6, s22, 4
	s_and_b32 s6, s6, 0x380
	s_add_u32 s6, s58, s6
	s_addc_u32 s7, s59, 0
	s_add_u32 s37, s6, 0x9400000
	s_addc_u32 s38, s7, 0
	s_add_u32 s39, s6, 0xac00200
	s_addc_u32 s40, s7, 0
	s_or_b32 s2, s2, s14
	s_add_u32 s2, s58, s2
	s_addc_u32 s3, s59, s3
	s_add_u32 s14, s2, 0xa408000
	s_addc_u32 s15, s3, 0
	s_add_u32 s16, s2, 0xa408100
	s_addc_u32 s17, s3, 0
	v_mov_b32_e32 v1, 0x42700000
	s_add_u32 s18, s2, 0xa5d8000
	v_cmp_le_f32_e64 s[4:5], s34, v1
	s_addc_u32 s19, s3, 0
	s_mov_b32 s41, 0
	s_mov_b64 s[20:21], -1
	v_readfirstlane_b32 s93, v0
	s_nop 3
	s_lshr_b32 s93, s93, 6
	s_cmp_lt_u32 s93, 4
	s_cbranch_scc0 .Lattn_prio_done
	s_setprio 1
